# v55 + P12 diff-attention softmax row sums via v_pk_add_f32 (32 serial f32 adds -> 14 packed + 3 scalar, f32 accumulation kept, summation order changed)
# baseline (speedup 1.0000x reference)
; template <int MODE, int DQK, int DV>
; __device__ __forceinline__ void attn_pass(LAS unsigned char* lds, const Tens& T, size_t rowbase, int q0, f32x16 (&o)[DV / 32], float& l_out, const int wave, QPre* qp = nullptr) {
;     ...
;             psum = 0.f;
; #pragma unroll
;             for (int rg = 0; rg < 16; ++rg) { const float e0 = __builtin_amdgcn_exp2f(p[0][rg]), e1 = __builtin_amdgcn_exp2f(p[1][rg]); p[0][rg] = e0; p[1][rg] = e1; psum += e0; psum += e1; }
;             if (!POSTHOC || redo) break;
;             if (__builtin_expect(!__any(!(psum <= BIG)), 1)) break;
;             redo = true;
.LBB0_2451:
	s_nop 4
	v_exp_f32_e32 v13, v96
	s_nop 0
	v_exp_f32_e32 v3, v112
	v_exp_f32_e32 v15, v97
	v_exp_f32_e32 v4, v113
	v_exp_f32_e32 v97, v98
	v_exp_f32_e32 v5, v114
	v_exp_f32_e32 v99, v99
	v_exp_f32_e32 v6, v115
	v_exp_f32_e32 v112, v100
	v_exp_f32_e32 v7, v116
	v_exp_f32_e32 v113, v101
	v_exp_f32_e32 v8, v117
	v_exp_f32_e32 v114, v102
	v_exp_f32_e32 v9, v118
	v_exp_f32_e32 v115, v103
	v_exp_f32_e32 v11, v119
	v_exp_f32_e32 v103, v104
	v_exp_f32_e32 v10, v120
	v_exp_f32_e32 v104, v105
	v_exp_f32_e32 v12, v121
	v_exp_f32_e32 v105, v106
	v_exp_f32_e32 v14, v122
	v_exp_f32_e32 v106, v107
	v_exp_f32_e32 v96, v123
	v_exp_f32_e32 v107, v108
	v_exp_f32_e32 v98, v124
	v_exp_f32_e32 v108, v109
	v_exp_f32_e32 v100, v125
	v_exp_f32_e32 v109, v110
	v_exp_f32_e32 v101, v126
	v_exp_f32_e32 v110, v111
	v_exp_f32_e32 v102, v127
	s_xor_b64 s[2:3], s[72:73], -1
	v_pk_add_f32 v[116:117], v[4:5], v[6:7]
	v_pk_add_f32 v[118:119], v[112:113], v[8:9]
	v_pk_add_f32 v[116:117], v[116:117], v[114:115]
	v_pk_add_f32 v[118:119], v[118:119], v[10:11]
	v_pk_add_f32 v[116:117], v[116:117], v[12:13]
	v_pk_add_f32 v[118:119], v[118:119], v[104:105]
	v_pk_add_f32 v[116:117], v[116:117], v[14:15]
	v_pk_add_f32 v[118:119], v[118:119], v[96:97]
	v_pk_add_f32 v[116:117], v[116:117], v[106:107]
	v_pk_add_f32 v[118:119], v[118:119], v[98:99]
	v_pk_add_f32 v[116:117], v[116:117], v[108:109]
	v_pk_add_f32 v[118:119], v[118:119], v[100:101]
	v_pk_add_f32 v[116:117], v[116:117], v[102:103]
	v_pk_add_f32 v[116:117], v[116:117], v[118:119]
	v_add_f32_e32 v2, v116, v117
	v_add_f32_e32 v2, v3, v2
	v_add_f32_e32 v2, v110, v2
	s_mov_b64 s[72:73], -1
	s_andn2_b64 vcc, exec, s[2:3]
	s_mov_b64 s[2:3], -1
	s_cbranch_vccnz .LBB0_2446
	v_cmp_nge_f32_e32 vcc, s88, v2
	s_cmp_eq_u64 vcc, 0
	s_cselect_b64 s[2:3], -1, 0
	s_branch .LBB0_2446
